# final4 + diff attention exp/PV section rewritten chunk-major (exp, cvt, rowsum of key-chunk c+1 issued between the PV MFMAs of chunk c; same math order)
# speedup vs baseline: 1.0063x; 1.0006x over previous
; template <int KS> DI void at_qk(f32x16& p0, f32x16& p1, LAS const unsigned char* Kt, int mapB, const bf16x8 (&qr)[8], float init, int r32, int hi) {
;     ...
;     for (int d0 = 0; d0 < KS; ++d0) { const int cb = mapB + (d0 * 16 + hi * 8) * 2;
;         kb[d0][0] = *(const LAS bf16x8*)(Kt + AT_KSWZ(r32, cb)); kb[d0][1] = *(const LAS bf16x8*)(Kt + AT_KSWZ(32 + r32, cb)); }
;     __builtin_amdgcn_sched_barrier(0);
; #pragma unroll
;     for (int d0 = 0; d0 < KS; ++d0) { p0 = MFMA32(kb[d0][0], qr[d0], p0); p1 = MFMA32(kb[d0][1], qr[d0], p1); }
; }
; DI float at_softmax(f32x16& p0, f32x16& p1, float& m_run, bool first, bool nearb, LAS const float* tabp, int lane) {
;     if (nearb) {
; #pragma unroll
;         for (int i = 0; i < 16; ++i) { p0[i] += tabp[8 * (i >> 2) + (i & 3)]; p1[i] += tabp[32 + 8 * (i >> 2) + (i & 3)]; }
;     }
;     float mx = p0[0];
; #pragma unroll
;     for (int i = 1; i < 16; ++i) mx = fmaxf(mx, p0[i]);
; #pragma unroll
;     for (int i = 0; i < 16; ++i) mx = fmaxf(mx, p1[i]);
;     float alpha = 1.f;
;     if (first || !__all(mx <= AT_THR)) {
;         mx = max_x32(mx, lane);
;         const float dl = first ? mx : fmaxf(mx, 0.f);
;         alpha = first ? 1.f : __builtin_amdgcn_exp2f(-dl); m_run += dl;
; #pragma unroll
;         for (int i = 0; i < 16; ++i) { p0[i] -= dl; p1[i] -= dl; }
;     }
; #pragma unroll
;     for (int i = 0; i < 16; ++i) p0[i] = __builtin_amdgcn_exp2f(p0[i]);
; #pragma unroll
;     for (int i = 0; i < 16; ++i) p1[i] = __builtin_amdgcn_exp2f(p1[i]);
;     return alpha;
; }
; DI bf16x8 at_pack(const f32x16& p, int s8) {
;     u32x4 w; w.x = at_cvtpk(p[s8], p[s8 + 1]); w.y = at_cvtpk(p[s8 + 2], p[s8 + 3]); w.z = at_cvtpk(p[s8 + 4], p[s8 + 5]); w.w = at_cvtpk(p[s8 + 6], p[s8 + 7]);
;     return __builtin_bit_cast(bf16x8, w);
; }
; template <int D0> DI void at_pv_block(f32x16 (&o)[4], int vb, const bf16x8 (&pf)[4]) {
;     const s16x4 l0 = at_tr_read<D0 * 512 + 0 * 4096>(vb), h0 = at_tr_read<D0 * 512 + 0 * 4096 + 2048>(vb), l1 = at_tr_read<D0 * 512 + 1 * 4096>(vb), h1 = at_tr_read<D0 * 512 + 1 * 4096 + 2048>(vb);
;     const s16x4 l2 = at_tr_read<D0 * 512 + 2 * 4096>(vb), h2 = at_tr_read<D0 * 512 + 2 * 4096 + 2048>(vb), l3 = at_tr_read<D0 * 512 + 3 * 4096>(vb), h3 = at_tr_read<D0 * 512 + 3 * 4096 + 2048>(vb);
;     asm volatile("s_waitcnt lgkmcnt(0)" ::: "memory"); __builtin_amdgcn_sched_barrier(0);
.LBB0_801:
	v_subrev_u32_e32 v87, s57, v160
	v_add_u32_e32 v87, s49, v87
	ds_read_b64_tr_b16 v[170:171], v87 offset:0x0
	ds_read_b64_tr_b16 v[172:173], v87 offset:0x800
	ds_read_b64_tr_b16 v[174:175], v87 offset:0x200
	ds_read_b64_tr_b16 v[176:177], v87 offset:0xa00
	ds_read_b64_tr_b16 v[178:179], v87 offset:0x400
	ds_read_b64_tr_b16 v[180:181], v87 offset:0xc00
	ds_read_b64_tr_b16 v[182:183], v87 offset:0x600
	ds_read_b64_tr_b16 v[184:185], v87 offset:0xe00
	v_exp_f32_e32 v112, v112
	v_exp_f32_e32 v113, v113
	v_exp_f32_e32 v114, v114
	v_exp_f32_e32 v115, v115
	v_exp_f32_e32 v116, v116
	v_exp_f32_e32 v117, v117
	v_exp_f32_e32 v118, v118
	v_exp_f32_e32 v119, v119
	v_cvt_pk_bf16_f32 v2, v112, v113
	v_cvt_pk_bf16_f32 v3, v114, v115
	v_cvt_pk_bf16_f32 v4, v116, v117
	v_cvt_pk_bf16_f32 v5, v118, v119
	v_add_f32_e32 v81, v112, v113
	v_add_f32_e32 v82, v114, v115
	v_add_f32_e32 v83, v116, v117
	v_add_f32_e32 v84, v118, v119
	v_add_f32_e32 v81, v81, v82
	v_add_f32_e32 v83, v83, v84
	v_add_f32_e32 v81, v81, v83
	v_add_f32_e32 v80, v80, v81
	s_waitcnt lgkmcnt(0)
	ds_read_b64_tr_b16 v[112:113], v87 offset:0x1000
	ds_read_b64_tr_b16 v[114:115], v87 offset:0x1800
	ds_read_b64_tr_b16 v[116:117], v87 offset:0x1200
	ds_read_b64_tr_b16 v[118:119], v87 offset:0x1a00
	ds_read_b64_tr_b16 v[88:89], v87 offset:0x1400
	ds_read_b64_tr_b16 v[90:91], v87 offset:0x1c00
	ds_read_b64_tr_b16 v[92:93], v87 offset:0x1600
	ds_read_b64_tr_b16 v[94:95], v87 offset:0x1e00
	v_mfma_f32_32x32x16_bf16 v[64:79], v[170:173], v[2:5], v[64:79]
	v_exp_f32_e32 v120, v120
	v_exp_f32_e32 v121, v121
	v_mfma_f32_32x32x16_bf16 v[48:63], v[174:177], v[2:5], v[48:63]
	v_exp_f32_e32 v122, v122
	v_exp_f32_e32 v123, v123
	v_mfma_f32_32x32x16_bf16 v[32:47], v[178:181], v[2:5], v[32:47]
	v_exp_f32_e32 v124, v124
	v_exp_f32_e32 v125, v125
	v_mfma_f32_32x32x16_bf16 v[16:31], v[182:185], v[2:5], v[16:31]
	v_exp_f32_e32 v126, v126
	v_exp_f32_e32 v127, v127
	v_cvt_pk_bf16_f32 v6, v120, v121
	v_cvt_pk_bf16_f32 v7, v122, v123
	v_cvt_pk_bf16_f32 v8, v124, v125
	v_cvt_pk_bf16_f32 v9, v126, v127
	v_add_f32_e32 v81, v120, v121
	v_add_f32_e32 v82, v122, v123
	v_add_f32_e32 v83, v124, v125
	v_add_f32_e32 v84, v126, v127
	v_add_f32_e32 v81, v81, v82
	v_add_f32_e32 v83, v83, v84
	v_add_f32_e32 v81, v81, v83
	v_add_f32_e32 v80, v80, v81
	s_waitcnt lgkmcnt(0)
	ds_read_b64_tr_b16 v[170:171], v87 offset:0x2000
	ds_read_b64_tr_b16 v[172:173], v87 offset:0x2800
	ds_read_b64_tr_b16 v[174:175], v87 offset:0x2200
	ds_read_b64_tr_b16 v[176:177], v87 offset:0x2a00
	ds_read_b64_tr_b16 v[178:179], v87 offset:0x2400
	ds_read_b64_tr_b16 v[180:181], v87 offset:0x2c00
	ds_read_b64_tr_b16 v[182:183], v87 offset:0x2600
	ds_read_b64_tr_b16 v[184:185], v87 offset:0x2e00
	v_mfma_f32_32x32x16_bf16 v[64:79], v[112:115], v[6:9], v[64:79]
	v_exp_f32_e32 v96, v96
	v_exp_f32_e32 v97, v97
	v_mfma_f32_32x32x16_bf16 v[48:63], v[116:119], v[6:9], v[48:63]
	v_exp_f32_e32 v98, v98
	v_exp_f32_e32 v99, v99
	v_mfma_f32_32x32x16_bf16 v[32:47], v[88:91], v[6:9], v[32:47]
	v_exp_f32_e32 v100, v100
	v_exp_f32_e32 v101, v101
	v_mfma_f32_32x32x16_bf16 v[16:31], v[92:95], v[6:9], v[16:31]
	v_exp_f32_e32 v102, v102
	v_exp_f32_e32 v103, v103
	v_cvt_pk_bf16_f32 v10, v96, v97
	v_cvt_pk_bf16_f32 v11, v98, v99
	v_cvt_pk_bf16_f32 v12, v100, v101
	v_cvt_pk_bf16_f32 v13, v102, v103
	v_add_f32_e32 v81, v96, v97
	v_add_f32_e32 v82, v98, v99
	v_add_f32_e32 v83, v100, v101
	v_add_f32_e32 v84, v102, v103
	v_add_f32_e32 v81, v81, v82
	v_add_f32_e32 v83, v83, v84
	v_add_f32_e32 v81, v81, v83
	v_add_f32_e32 v80, v80, v81
	s_waitcnt lgkmcnt(0)
	ds_read_b64_tr_b16 v[112:113], v87 offset:0x3000
	ds_read_b64_tr_b16 v[114:115], v87 offset:0x3800
	ds_read_b64_tr_b16 v[116:117], v87 offset:0x3200
	ds_read_b64_tr_b16 v[118:119], v87 offset:0x3a00
	ds_read_b64_tr_b16 v[88:89], v87 offset:0x3400
	ds_read_b64_tr_b16 v[90:91], v87 offset:0x3c00
	ds_read_b64_tr_b16 v[92:93], v87 offset:0x3600
	ds_read_b64_tr_b16 v[94:95], v87 offset:0x3e00
	v_mfma_f32_32x32x16_bf16 v[64:79], v[170:173], v[10:13], v[64:79]
	v_exp_f32_e32 v104, v104
	v_exp_f32_e32 v105, v105
	v_mfma_f32_32x32x16_bf16 v[48:63], v[174:177], v[10:13], v[48:63]
	v_exp_f32_e32 v106, v106
	v_exp_f32_e32 v107, v107
	v_mfma_f32_32x32x16_bf16 v[32:47], v[178:181], v[10:13], v[32:47]
	v_exp_f32_e32 v108, v108
	v_exp_f32_e32 v109, v109
	v_mfma_f32_32x32x16_bf16 v[16:31], v[182:185], v[10:13], v[16:31]
	v_exp_f32_e32 v110, v110
	v_exp_f32_e32 v111, v111
	v_cvt_pk_bf16_f32 v166, v104, v105
	v_cvt_pk_bf16_f32 v167, v106, v107
	v_cvt_pk_bf16_f32 v168, v108, v109
	v_cvt_pk_bf16_f32 v169, v110, v111
	v_add_f32_e32 v81, v104, v105
	v_add_f32_e32 v82, v106, v107
	v_add_f32_e32 v83, v108, v109
	v_add_f32_e32 v84, v110, v111
	v_add_f32_e32 v81, v81, v82
	v_add_f32_e32 v83, v83, v84
	v_add_f32_e32 v81, v81, v83
	v_add_f32_e32 v80, v80, v81
	s_waitcnt lgkmcnt(0)
	v_mfma_f32_32x32x16_bf16 v[64:79], v[112:115], v[166:169], v[64:79]
	v_mfma_f32_32x32x16_bf16 v[48:63], v[116:119], v[166:169], v[48:63]
	v_mfma_f32_32x32x16_bf16 v[32:47], v[88:91], v[166:169], v[32:47]
	v_mfma_f32_32x32x16_bf16 v[16:31], v[92:95], v[166:169], v[16:31]
	s_mov_b64 s[38:39], 0
	s_mov_b64 s[58:59], -1
	s_and_b64 vcc, exec, s[40:41]
	s_cbranch_vccz .LBB0_790

; template <int KS> DI void at_qk(f32x16& p0, f32x16& p1, LAS const unsigned char* Kt, int mapB, const bf16x8 (&qr)[8], float init, int r32, int hi) {
;     ...
;     for (int d0 = 0; d0 < KS; ++d0) { const int cb = mapB + (d0 * 16 + hi * 8) * 2;
;         kb[d0][0] = *(const LAS bf16x8*)(Kt + AT_KSWZ(r32, cb)); kb[d0][1] = *(const LAS bf16x8*)(Kt + AT_KSWZ(32 + r32, cb)); }
;     __builtin_amdgcn_sched_barrier(0);
; #pragma unroll
;     for (int d0 = 0; d0 < KS; ++d0) { p0 = MFMA32(kb[d0][0], qr[d0], p0); p1 = MFMA32(kb[d0][1], qr[d0], p1); }
; }
; DI float at_softmax(f32x16& p0, f32x16& p1, float& m_run, bool first, bool nearb, LAS const float* tabp, int lane) {
;     if (nearb) {
; #pragma unroll
;         for (int i = 0; i < 16; ++i) { p0[i] += tabp[8 * (i >> 2) + (i & 3)]; p1[i] += tabp[32 + 8 * (i >> 2) + (i & 3)]; }
;     }
;     float mx = p0[0];
; #pragma unroll
;     for (int i = 1; i < 16; ++i) mx = fmaxf(mx, p0[i]);
; #pragma unroll
;     for (int i = 0; i < 16; ++i) mx = fmaxf(mx, p1[i]);
;     float alpha = 1.f;
;     if (first || !__all(mx <= AT_THR)) {
;         mx = max_x32(mx, lane);
;         const float dl = first ? mx : fmaxf(mx, 0.f);
;         alpha = first ? 1.f : __builtin_amdgcn_exp2f(-dl); m_run += dl;
; #pragma unroll
;         for (int i = 0; i < 16; ++i) { p0[i] -= dl; p1[i] -= dl; }
;     }
; #pragma unroll
;     for (int i = 0; i < 16; ++i) p0[i] = __builtin_amdgcn_exp2f(p0[i]);
; #pragma unroll
;     for (int i = 0; i < 16; ++i) p1[i] = __builtin_amdgcn_exp2f(p1[i]);
;     return alpha;
; }
; DI bf16x8 at_pack(const f32x16& p, int s8) {
;     u32x4 w; w.x = at_cvtpk(p[s8], p[s8 + 1]); w.y = at_cvtpk(p[s8 + 2], p[s8 + 3]); w.z = at_cvtpk(p[s8 + 4], p[s8 + 5]); w.w = at_cvtpk(p[s8 + 6], p[s8 + 7]);
;     return __builtin_bit_cast(bf16x8, w);
; }
; template <int D0> DI void at_pv_block(f32x16 (&o)[4], int vb, const bf16x8 (&pf)[4]) {
;     const s16x4 l0 = at_tr_read<D0 * 512 + 0 * 4096>(vb), h0 = at_tr_read<D0 * 512 + 0 * 4096 + 2048>(vb), l1 = at_tr_read<D0 * 512 + 1 * 4096>(vb), h1 = at_tr_read<D0 * 512 + 1 * 4096 + 2048>(vb);
;     const s16x4 l2 = at_tr_read<D0 * 512 + 2 * 4096>(vb), h2 = at_tr_read<D0 * 512 + 2 * 4096 + 2048>(vb), l3 = at_tr_read<D0 * 512 + 3 * 4096>(vb), h3 = at_tr_read<D0 * 512 + 3 * 4096 + 2048>(vb);
;     asm volatile("s_waitcnt lgkmcnt(0)" ::: "memory"); __builtin_amdgcn_sched_barrier(0);
.LBB0_844:
	v_subrev_u32_e32 v87, s48, v160
	v_add_u32_e32 v87, s31, v87
	ds_read_b64_tr_b16 v[170:171], v87 offset:0x0
	ds_read_b64_tr_b16 v[172:173], v87 offset:0x800
	ds_read_b64_tr_b16 v[174:175], v87 offset:0x200
	ds_read_b64_tr_b16 v[176:177], v87 offset:0xa00
	ds_read_b64_tr_b16 v[178:179], v87 offset:0x400
	ds_read_b64_tr_b16 v[180:181], v87 offset:0xc00
	ds_read_b64_tr_b16 v[182:183], v87 offset:0x600
	ds_read_b64_tr_b16 v[184:185], v87 offset:0xe00
	v_exp_f32_e32 v112, v112
	v_exp_f32_e32 v113, v113
	v_exp_f32_e32 v114, v114
	v_exp_f32_e32 v115, v115
	v_exp_f32_e32 v116, v116
	v_exp_f32_e32 v117, v117
	v_exp_f32_e32 v118, v118
	v_exp_f32_e32 v119, v119
	v_cvt_pk_bf16_f32 v2, v112, v113
	v_cvt_pk_bf16_f32 v3, v114, v115
	v_cvt_pk_bf16_f32 v4, v116, v117
	v_cvt_pk_bf16_f32 v5, v118, v119
	v_add_f32_e32 v81, v112, v113
	v_add_f32_e32 v82, v114, v115
	v_add_f32_e32 v83, v116, v117
	v_add_f32_e32 v84, v118, v119
	v_add_f32_e32 v81, v81, v82
	v_add_f32_e32 v83, v83, v84
	v_add_f32_e32 v81, v81, v83
	v_add_f32_e32 v80, v80, v81
	s_waitcnt lgkmcnt(0)
	ds_read_b64_tr_b16 v[112:113], v87 offset:0x1000
	ds_read_b64_tr_b16 v[114:115], v87 offset:0x1800
	ds_read_b64_tr_b16 v[116:117], v87 offset:0x1200
	ds_read_b64_tr_b16 v[118:119], v87 offset:0x1a00
	ds_read_b64_tr_b16 v[88:89], v87 offset:0x1400
	ds_read_b64_tr_b16 v[90:91], v87 offset:0x1c00
	ds_read_b64_tr_b16 v[92:93], v87 offset:0x1600
	ds_read_b64_tr_b16 v[94:95], v87 offset:0x1e00
	v_mfma_f32_32x32x16_bf16 v[64:79], v[170:173], v[2:5], v[64:79]
	v_exp_f32_e32 v120, v120
	v_exp_f32_e32 v121, v121
	v_mfma_f32_32x32x16_bf16 v[48:63], v[174:177], v[2:5], v[48:63]
	v_exp_f32_e32 v122, v122
	v_exp_f32_e32 v123, v123
	v_mfma_f32_32x32x16_bf16 v[32:47], v[178:181], v[2:5], v[32:47]
	v_exp_f32_e32 v124, v124
	v_exp_f32_e32 v125, v125
	v_mfma_f32_32x32x16_bf16 v[16:31], v[182:185], v[2:5], v[16:31]
	v_exp_f32_e32 v126, v126
	v_exp_f32_e32 v127, v127
	v_cvt_pk_bf16_f32 v6, v120, v121
	v_cvt_pk_bf16_f32 v7, v122, v123
	v_cvt_pk_bf16_f32 v8, v124, v125
	v_cvt_pk_bf16_f32 v9, v126, v127
	v_add_f32_e32 v81, v120, v121
	v_add_f32_e32 v82, v122, v123
	v_add_f32_e32 v83, v124, v125
	v_add_f32_e32 v84, v126, v127
	v_add_f32_e32 v81, v81, v82
	v_add_f32_e32 v83, v83, v84
	v_add_f32_e32 v81, v81, v83
	v_add_f32_e32 v80, v80, v81
	s_waitcnt lgkmcnt(0)
	ds_read_b64_tr_b16 v[170:171], v87 offset:0x2000
	ds_read_b64_tr_b16 v[172:173], v87 offset:0x2800
	ds_read_b64_tr_b16 v[174:175], v87 offset:0x2200
	ds_read_b64_tr_b16 v[176:177], v87 offset:0x2a00
	ds_read_b64_tr_b16 v[178:179], v87 offset:0x2400
	ds_read_b64_tr_b16 v[180:181], v87 offset:0x2c00
	ds_read_b64_tr_b16 v[182:183], v87 offset:0x2600
	ds_read_b64_tr_b16 v[184:185], v87 offset:0x2e00
	v_mfma_f32_32x32x16_bf16 v[64:79], v[112:115], v[6:9], v[64:79]
	v_exp_f32_e32 v96, v96
	v_exp_f32_e32 v97, v97
	v_mfma_f32_32x32x16_bf16 v[48:63], v[116:119], v[6:9], v[48:63]
	v_exp_f32_e32 v98, v98
	v_exp_f32_e32 v99, v99
	v_mfma_f32_32x32x16_bf16 v[32:47], v[88:91], v[6:9], v[32:47]
	v_exp_f32_e32 v100, v100
	v_exp_f32_e32 v101, v101
	v_mfma_f32_32x32x16_bf16 v[16:31], v[92:95], v[6:9], v[16:31]
	v_exp_f32_e32 v102, v102
	v_exp_f32_e32 v103, v103
	v_cvt_pk_bf16_f32 v10, v96, v97
	v_cvt_pk_bf16_f32 v11, v98, v99
	v_cvt_pk_bf16_f32 v12, v100, v101
	v_cvt_pk_bf16_f32 v13, v102, v103
	v_add_f32_e32 v81, v96, v97
	v_add_f32_e32 v82, v98, v99
	v_add_f32_e32 v83, v100, v101
	v_add_f32_e32 v84, v102, v103
	v_add_f32_e32 v81, v81, v82
	v_add_f32_e32 v83, v83, v84
	v_add_f32_e32 v81, v81, v83
	v_add_f32_e32 v80, v80, v81
	s_waitcnt lgkmcnt(0)
	ds_read_b64_tr_b16 v[112:113], v87 offset:0x3000
	ds_read_b64_tr_b16 v[114:115], v87 offset:0x3800
	ds_read_b64_tr_b16 v[116:117], v87 offset:0x3200
	ds_read_b64_tr_b16 v[118:119], v87 offset:0x3a00
	ds_read_b64_tr_b16 v[88:89], v87 offset:0x3400
	ds_read_b64_tr_b16 v[90:91], v87 offset:0x3c00
	ds_read_b64_tr_b16 v[92:93], v87 offset:0x3600
	ds_read_b64_tr_b16 v[94:95], v87 offset:0x3e00
	v_mfma_f32_32x32x16_bf16 v[64:79], v[170:173], v[10:13], v[64:79]
	v_exp_f32_e32 v104, v104
	v_exp_f32_e32 v105, v105
	v_mfma_f32_32x32x16_bf16 v[48:63], v[174:177], v[10:13], v[48:63]
	v_exp_f32_e32 v106, v106
	v_exp_f32_e32 v107, v107
	v_mfma_f32_32x32x16_bf16 v[32:47], v[178:181], v[10:13], v[32:47]
	v_exp_f32_e32 v108, v108
	v_exp_f32_e32 v109, v109
	v_mfma_f32_32x32x16_bf16 v[16:31], v[182:185], v[10:13], v[16:31]
	v_exp_f32_e32 v110, v110
	v_exp_f32_e32 v111, v111
	v_cvt_pk_bf16_f32 v166, v104, v105
	v_cvt_pk_bf16_f32 v167, v106, v107
	v_cvt_pk_bf16_f32 v168, v108, v109
	v_cvt_pk_bf16_f32 v169, v110, v111
	v_add_f32_e32 v81, v104, v105
	v_add_f32_e32 v82, v106, v107
	v_add_f32_e32 v83, v108, v109
	v_add_f32_e32 v84, v110, v111
	v_add_f32_e32 v81, v81, v82
	v_add_f32_e32 v83, v83, v84
	v_add_f32_e32 v81, v81, v83
	v_add_f32_e32 v80, v80, v81
	s_waitcnt lgkmcnt(0)
	v_mfma_f32_32x32x16_bf16 v[64:79], v[112:115], v[166:169], v[64:79]
	v_mfma_f32_32x32x16_bf16 v[48:63], v[116:119], v[166:169], v[48:63]
	v_mfma_f32_32x32x16_bf16 v[32:47], v[88:91], v[166:169], v[32:47]
	v_mfma_f32_32x32x16_bf16 v[16:31], v[92:95], v[166:169], v[16:31]
	s_mov_b64 s[42:43], 0
	s_mov_b64 s[58:59], -1
	s_and_b64 vcc, exec, s[76:77]
	s_cbranch_vccz .LBB0_833
